# P7 main K loop: A-staging LDS-DMA addresses from one scalar base per step plus the 32-bit row offset (no 64-bit VALU add per DMA)
# speedup vs baseline: 1.0037x; 1.0029x over previous
; #define MG_STAGE_A(b, rows, k0) do { _Pragma("unroll") for (int h_ = 0; h_ < 2; ++h_) _Pragma("unroll") for (int i_ = 0; i_ < 2; ++i_) if (rows[h_][i_] != 0xffffffffu) \
;         __builtin_amdgcn_global_load_lds((const unsigned*)((const char*)Abase + rows[h_][i_] + (k0) * 2), (PG8_LAS unsigned*)(lds + MG_SA(b, h_) + ldsw + i_ * 8192), 16, 0, 0); } while (0)
; #define MG_LDB(dst, b, h) do { _Pragma("unroll") for (int n = 0; n < 2; ++n) _Pragma("unroll") for (int k = 0; k < 2; ++k) dst[n][k] = *(const PG8_LAS bf16x8*)(lds + MG_SB(b, h) + boff + n * 2048 + k * 1024); } while (0)
; template <class Epi, bool G1> ...
;     ...
;         for (int t = 0; t < NT; ++t) {
;             const bool last = (t == NT - 1), more = !last || has_next;
;             if (wact) { MG_LDB(B0, buf, 0); MG_LDB(B1, buf, 1); }
;             if (!last) { MG_STAGE_A(buf ^ 1, rowC, (t + 1) * BK); }
;             else if (has_next) { MG_ROWS(nxt, rowC); MG_STAGE_A(buf ^ 1, rowC, 0); }
.LBB0_1075:
	v_cndmask_b32_e64 v203, 0, 1, s[36:37]
	s_mov_b32 s70, s46
	s_add_u32 s74, s44, 0x70000080
	s_addc_u32 s75, s45, 0
	v_cmp_ne_u32_e64 s[10:11], 1, v203
	s_andn2_b64 vcc, exec, s[36:37]
	s_lshl_b32 s71, s46, 15
	s_cbranch_vccz .LBB0_1082
	s_xor_b32 s72, s71, 0x8000
	s_and_saveexec_b64 s[46:47], s[14:15]
	s_cbranch_execnz .LBB0_1083

; #define MG_STAGE_A(b, rows, k0) do { _Pragma("unroll") for (int h_ = 0; h_ < 2; ++h_) _Pragma("unroll") for (int i_ = 0; i_ < 2; ++i_) if (rows[h_][i_] != 0xffffffffu) \
;         __builtin_amdgcn_global_load_lds((const unsigned*)((const char*)Abase + rows[h_][i_] + (k0) * 2), (PG8_LAS unsigned*)(lds + MG_SA(b, h_) + ldsw + i_ * 8192), 16, 0, 0); } while (0)
; template <class Epi, bool G1> ...
;     ...
;             if (!last) { MG_STAGE_A(buf ^ 1, rowC, (t + 1) * BK); }
.LBB0_1083:
	s_add_i32 m0, s51, s72
	s_nop 0
	global_load_lds_dwordx4 v194, s[74:75]
	s_or_b64 exec, exec, s[46:47]
	s_and_saveexec_b64 s[46:47], s[12:13]
	s_cbranch_execz .LBB0_1078
.LBB0_1084:
	s_add_i32 s73, s51, s72
	s_add_i32 m0, s73, 0x2000
	s_nop 0
	global_load_lds_dwordx4 v192, s[74:75]
	s_or_b64 exec, exec, s[46:47]
	s_and_saveexec_b64 s[46:47], s[8:9]
	s_cbranch_execz .LBB0_1079
.LBB0_1085:
	s_add_i32 s73, s51, s72
	s_add_i32 m0, s73, 0x4000
	s_nop 0
	global_load_lds_dwordx4 v198, s[74:75]
	s_or_b64 exec, exec, s[46:47]
	s_and_saveexec_b64 s[46:47], s[6:7]
	s_cbranch_execz .LBB0_1080
.LBB0_1086:
	s_add_i32 s73, s51, s72
	s_add_i32 m0, s73, 0x6000
	s_nop 0
	global_load_lds_dwordx4 v196, s[74:75]
	s_or_b64 exec, exec, s[46:47]
	s_and_b64 vcc, exec, s[10:11]
	s_cbranch_vccnz .LBB0_1081
